# s16
# speedup vs baseline: 1.0141x; 1.0141x over previous
_Z11attn_kernelILi4EEvPKfS1_S1_S1_S1_S1_PKcPf:
	s_load_dwordx2 s[24:25], s[0:1], 0x30
	s_load_dwordx8 s[8:15], s[0:1], 0x0
	s_load_dwordx4 s[16:19], s[0:1], 0x20
	v_lshrrev_b32_e32 v63, 6, v0
	v_and_b32_e32 v57, 15, v0
	v_bfe_u32 v1, v0, 4, 2
	v_lshrrev_b32_e32 v2, 2, v57
	v_mul_u32_u24_e32 v4, 3, v1
	v_mul_u32_u24_e32 v2, 3, v2
	v_mad_u32_u24 v4, v63, 12, v4
	v_mad_u32_u24 v2, v63, 12, v2
	v_lshlrev_b32_e32 v4, 2, v4
	v_lshlrev_b32_e32 v2, 2, v2
	v_and_b32_e32 v104, 63, v0
	v_lshlrev_b32_e32 v60, 5, v57
	v_lshlrev_b32_e32 v58, 3, v1
	v_add_u32_e32 v3, v60, v58
	v_lshrrev_b32_e32 v56, 4, v0
	v_lshlrev_b32_e32 v54, 4, v57
	v_mov_b32_e32 v59, 0
	s_movk_i32 s4, 0xe0
	v_cmp_gt_u32_e64 s[4:5], s4, v0
	s_lshl_b32 s26, s2, 8
	s_lshl_b32 s27, s2, 9
	s_mul_i32 s28, s2, 14
	s_add_u32 s26, s26, 0x164000
	s_add_u32 s27, s27, 0x80000
	s_add_u32 s20, s26, 0xc0
	v_lshlrev_b32_e32 v5, 2, v57
	v_lshlrev_b32_e32 v147, 6, v57
	v_add_u32_e32 v2, s26, v2
	v_add_u32_e32 v4, s26, v4
	v_add_u32_e32 v3, s27, v3
	v_mul_u32_u24_e32 v156, 0x140, v1
	s_movk_i32 s21, 0x500
	v_mad_u32_u24 v156, v63, s21, v156
	v_lshl_or_b32 v156, v57, 2, v156
	v_add_u32_e32 v156, 0x1c00, v156
	v_lshlrev_b32_e32 v157, 5, v56
	v_cmp_gt_u32_e32 vcc, 3, v57
	v_add_u32_e32 v158, 4, v57
	v_lshlrev_b32_e32 v159, 2, v57
	s_movk_i32 s21, 0x50
	v_cndmask_b32_e32 v158, 4, v158, vcc
	v_mad_u32_u24 v159, v56, s21, v159
	v_lshl_add_u32 v158, v158, 2, v157
	v_mul_u32_u24_e32 v250, 0x50, v56
	v_or_b32_e32 v250, 0x3800, v250
	v_lshl_add_u32 v251, v57, 1, v250
	v_mul_u32_u24_e32 v252, 0x50, v57
	v_lshl_add_u32 v252, v58, 1, v252
	v_lshlrev_b32_e32 v253, 2, v57
	v_and_b32_e32 v254, 0xc0, v0
	v_lshlrev_b32_e32 v255, 11, v1
	v_or3_b32 v253, v253, v254, v255
	v_add_u32_e32 v254, s28, v56
	v_lshl_add_u32 v254, v254, 9, v54
	v_lshl_or_b32 v255, v56, 9, v54
	s_waitcnt lgkmcnt(0)
	global_load_dwordx3 v[80:82], v2, s[24:25]
	global_load_dwordx3 v[84:86], v4, s[24:25]
	global_load_dwordx2 v[64:65], v3, s[24:25]
	s_load_dword s3, s[24:25], s20
	s_add_u32 s22, s24, 0x160000
	s_addc_u32 s23, s25, 0
	v_cndmask_b32_e64 v62, 13, v56, s[4:5]
	v_add_u32_e32 v3, s28, v62
	v_mad_u32_u24 v144, v3, 36, v5
	v_mad_u32_u24 v146, v3, 12, v5
	v_add_u32_e32 v145, -36, v146
	v_add_u32_e32 v146, -48, v146
	v_lshl_or_b32 v147, v63, 10, v147
	v_lshl_or_b32 v147, v1, 4, v147
	v_or_b32_e32 v148, 0x1000, v147
	v_lshlrev_b32_e32 v149, 4, v104
	v_lshlrev_b32_e32 v150, 9, v3
	v_add_u32_e32 v150, v150, v54
	v_and_b32_e32 v87, 3, v57
	v_lshlrev_b32_e32 v87, 4, v87
	v_lshl_or_b32 v87, v1, 6, v87
	v_lshlrev_b32_e32 v88, 3, v57
	s_add_u32 s26, s24, 0x100000
	s_addc_u32 s27, s25, 0
	s_add_u32 s28, s24, 0x140000
	s_addc_u32 s29, s25, 0
	s_movk_i32 s6, 0x140
	v_cmp_gt_u32_e32 vcc, s6, v0
	v_lshlrev_b32_e32 v22, 2, v0
	v_mov_b32_e32 v23, 0
	s_and_saveexec_b64 s[6:7], vcc
	ds_write_b32 v22, v23 offset:14336
	s_or_b64 exec, exec, s[6:7]
	v_cmp_gt_u32_e32 vcc, 64, v0
	s_and_saveexec_b64 s[6:7], vcc
	ds_write_b32 v22, v23 offset:15360
	s_or_b64 exec, exec, s[6:7]
	v_mov_b32_e32 v45, 0xc9c35000
	s_mov_b32 s30, 0x3db8aa3b
	s_mov_b32 s31, 0x3db8aa3b
	v_mov_b32_e32 v121, 0x3fb8aa3b
	v_mov_b32_e32 v35, 0
	v_mov_b32_e32 v44, v45
	s_waitcnt lgkmcnt(0)
	s_bitcmp0_b32 s3, 1
	s_cselect_b64 s[20:21], -1, 0
	s_cbranch_scc1 .LBB1_16
	v_bfe_u32 v22, s3, v57, 1
	v_cmp_eq_u32_e64 s[6:7], 0, v22
	s_bitcmp0_b32 s3, 0
	s_cselect_b64 vcc, -1, 0
	v_cndmask_b32_e32 v34, 0, v45, vcc
	v_cndmask_b32_e64 v55, 1.0, 0, s[6:7]
	s_bitcmp0_b32 s3, 2
	s_cselect_b64 vcc, -1, 0
	v_cndmask_b32_e32 v36, 0, v45, vcc
	s_bitcmp0_b32 s3, 3
	s_cselect_b64 vcc, -1, 0
	v_cndmask_b32_e32 v37, 0, v45, vcc
	s_bitcmp0_b32 s3, 4
	s_cselect_b64 vcc, -1, 0
	v_cndmask_b32_e32 v22, 0, v45, vcc
	s_bitcmp0_b32 s3, 5
	s_cselect_b64 vcc, -1, 0
	v_cndmask_b32_e32 v23, 0, v45, vcc
	s_bitcmp0_b32 s3, 6
	s_cselect_b64 vcc, -1, 0
	v_cndmask_b32_e32 v24, 0, v45, vcc
	s_bitcmp0_b32 s3, 7
	s_cselect_b64 vcc, -1, 0
	v_cndmask_b32_e32 v25, 0, v45, vcc
	s_bitcmp0_b32 s3, 8
	s_cselect_b64 vcc, -1, 0
	v_cndmask_b32_e32 v38, 0, v45, vcc
	s_bitcmp0_b32 s3, 9
	s_cselect_b64 vcc, -1, 0
	v_cndmask_b32_e32 v39, 0, v45, vcc
	s_bitcmp0_b32 s3, 10
	s_cselect_b64 vcc, -1, 0
	v_cndmask_b32_e32 v40, 0, v45, vcc
	s_bitcmp0_b32 s3, 11
	s_cselect_b64 vcc, -1, 0
	v_cndmask_b32_e32 v41, 0, v45, vcc
	s_bitcmp0_b32 s3, 12
	s_cselect_b64 vcc, -1, 0
	v_cndmask_b32_e32 v42, 0, v45, vcc
	s_bitcmp0_b32 s3, 13
	s_cselect_b64 vcc, -1, 0
	v_cndmask_b32_e32 v43, 0, v45, vcc
	s_waitcnt vmcnt(1)
	v_lshl_add_u32 v72, v80, 9, v87
	v_lshl_add_u32 v73, v81, 9, v87
	v_lshl_add_u32 v74, v82, 9, v87
	global_load_dwordx4 v[50:53], v72, s[24:25]
	global_load_dwordx4 v[46:49], v72, s[24:25] offset:256
	global_load_dwordx4 v[14:17], v73, s[24:25]
	global_load_dwordx4 v[10:13], v73, s[24:25] offset:256
	global_load_dwordx4 v[6:9], v74, s[24:25]
	global_load_dwordx4 v[2:5], v74, s[24:25] offset:256
	v_lshl_add_u32 v75, v84, 8, v54
	v_lshl_add_u32 v78, v84, 7, v88
	v_lshl_add_u32 v76, v85, 8, v54
	v_lshl_add_u32 v79, v85, 7, v88
	v_lshl_add_u32 v77, v86, 8, v54
	v_lshl_add_u32 v80, v86, 7, v88
	global_load_dwordx4 v[30:33], v75, s[26:27]
	global_load_dwordx2 v[70:71], v78, s[28:29]
	global_load_dwordx4 v[26:29], v76, s[26:27]
	global_load_dwordx2 v[66:67], v79, s[28:29]
	global_load_dwordx4 v[18:21], v77, s[26:27]
	global_load_dwordx2 v[68:69], v80, s[28:29]
	s_mov_b32 exec_lo, 0x1ff01ff
	s_mov_b32 exec_hi, 0x1ff01ff
	global_load_dword v120, v144, s[10:11]
	s_mov_b32 exec_lo, 0xe000e00
	s_mov_b32 exec_hi, 0xe000e00
	global_load_dword v120, v145, s[12:13]
	s_mov_b32 exec_lo, 0x70007000
	s_mov_b32 exec_hi, 0x70007000
	global_load_dword v120, v146, s[14:15]
	s_mov_b64 exec, -1
	global_load_dwordx4 v[124:127], v147, s[22:23]
	global_load_dwordx4 v[128:131], v148, s[22:23]
	s_mov_b32 exec_hi, 0
	global_load_dwordx4 v[132:135], v149, s[16:17]
	s_mov_b32 exec_hi, -1
	s_mov_b32 exec_lo, 0
	global_load_dwordx4 v[132:135], v149, s[18:19] offset:-512
	s_mov_b32 exec_lo, -1
	global_load_dwordx4 v[136:139], v150, s[8:9]
	global_load_dwordx4 v[140:143], v150, s[8:9] offset:256
	v_mov_b32_e32 v75, 0
	v_mov_b32_e32 v79, 0
	v_mov_b32_e32 v83, 0
	s_waitcnt vmcnt(20)
	v_mfma_f32_16x16x32_fp8_fp8 v[160:163], v[50:51], v[64:65], v[34:37]
	v_mfma_f32_16x16x32_fp8_fp8 v[164:167], v[52:53], v[64:65], v[22:25]
	s_waitcnt vmcnt(19)
	v_mfma_f32_16x16x32_fp8_fp8 v[168:171], v[46:47], v[64:65], v[38:41]
	v_mfma_f32_16x16x32_fp8_fp8 v[172:175], v[48:49], v[64:65], v[42:45]
	s_nop 3
	v_max3_f32 v86, v160, v161, v162
	v_max3_f32 v87, v163, v164, v165
	v_max3_f32 v88, v166, v167, v168
	v_max3_f32 v89, v169, v170, v171
	v_max3_f32 v86, v86, v172, v173
	v_max3_f32 v87, v87, v88, v89
	v_max_f32_e32 v96, v86, v87
	v_mul_f32_e32 v98, 0xbdb8aa3b, v96
	v_pk_fma_f32 v[208:209], v[160:161], s[30:31], v[98:99] op_sel_hi:[1,1,0]
	v_pk_fma_f32 v[210:211], v[162:163], s[30:31], v[98:99] op_sel_hi:[1,1,0]
	v_pk_fma_f32 v[212:213], v[164:165], s[30:31], v[98:99] op_sel_hi:[1,1,0]
	v_pk_fma_f32 v[214:215], v[166:167], s[30:31], v[98:99] op_sel_hi:[1,1,0]
	v_pk_fma_f32 v[216:217], v[168:169], s[30:31], v[98:99] op_sel_hi:[1,1,0]
	v_pk_fma_f32 v[218:219], v[170:171], s[30:31], v[98:99] op_sel_hi:[1,1,0]
	v_pk_fma_f32 v[220:221], v[172:173], s[30:31], v[98:99] op_sel_hi:[1,1,0]
	v_exp_f32_e32 v208, v208
	v_exp_f32_e32 v209, v209
	v_exp_f32_e32 v210, v210
	v_exp_f32_e32 v211, v211
	v_exp_f32_e32 v212, v212
	v_exp_f32_e32 v213, v213
	v_exp_f32_e32 v214, v214
	v_exp_f32_e32 v215, v215
	v_exp_f32_e32 v216, v216
	v_exp_f32_e32 v217, v217
	v_exp_f32_e32 v218, v218
	v_exp_f32_e32 v219, v219
	v_exp_f32_e32 v220, v220
	v_exp_f32_e32 v221, v221
	s_waitcnt vmcnt(18)
	v_mfma_f32_16x16x32_fp8_fp8 v[176:179], v[14:15], v[64:65], v[34:37]
	v_mfma_f32_16x16x32_fp8_fp8 v[180:183], v[16:17], v[64:65], v[22:25]
	s_waitcnt vmcnt(17)
	v_mfma_f32_16x16x32_fp8_fp8 v[184:187], v[10:11], v[64:65], v[38:41]
	v_mfma_f32_16x16x32_fp8_fp8 v[188:191], v[12:13], v[64:65], v[42:45]
	v_pk_add_f32 v[86:87], v[208:209], v[210:211]
	v_pk_add_f32 v[88:89], v[212:213], v[214:215]
	v_pk_add_f32 v[90:91], v[216:217], v[218:219]
	v_pk_mul_f32 v[92:93], v[208:209], v[160:161]
	v_pk_mul_f32 v[94:95], v[210:211], v[162:163]
	v_pk_add_f32 v[86:87], v[86:87], v[220:221]
	v_pk_add_f32 v[88:89], v[88:89], v[90:91]
	v_pk_fma_f32 v[92:93], v[212:213], v[164:165], v[92:93]
	v_pk_fma_f32 v[94:95], v[214:215], v[166:167], v[94:95]
	v_pk_add_f32 v[86:87], v[86:87], v[88:89]
	v_pk_fma_f32 v[92:93], v[216:217], v[168:169], v[92:93]
	v_pk_fma_f32 v[94:95], v[218:219], v[170:171], v[94:95]
	v_add_f32_e32 v86, v86, v87
	v_pk_fma_f32 v[92:93], v[220:221], v[172:173], v[92:93]
	v_rcp_f32_e32 v87, v86
	v_pk_add_f32 v[92:93], v[92:93], v[94:95]
	v_mul_f32_e32 v87, v55, v87
	v_add_f32_e32 v92, v92, v93
	v_mul_f32_e32 v107, v86, v87
	v_mul_f32_e32 v92, v92, v87
	v_mul_f32_e32 v100, 0x43800000, v87
	v_mul_f32_e32 v103, 0x3d800000, v92
	v_max3_f32 v86, v176, v177, v178
	v_max3_f32 v87, v179, v180, v181
	v_max3_f32 v88, v182, v183, v184
	v_max3_f32 v89, v185, v186, v187
	v_max3_f32 v86, v86, v188, v189
	v_max3_f32 v87, v87, v88, v89
	v_max_f32_e32 v96, v86, v87
	v_mul_f32_e32 v98, 0xbdb8aa3b, v96
	v_pk_fma_f32 v[222:223], v[176:177], s[30:31], v[98:99] op_sel_hi:[1,1,0]
	v_pk_fma_f32 v[224:225], v[178:179], s[30:31], v[98:99] op_sel_hi:[1,1,0]
	v_pk_fma_f32 v[226:227], v[180:181], s[30:31], v[98:99] op_sel_hi:[1,1,0]
	v_pk_fma_f32 v[228:229], v[182:183], s[30:31], v[98:99] op_sel_hi:[1,1,0]
	v_pk_fma_f32 v[230:231], v[184:185], s[30:31], v[98:99] op_sel_hi:[1,1,0]
	v_pk_fma_f32 v[232:233], v[186:187], s[30:31], v[98:99] op_sel_hi:[1,1,0]
	v_pk_fma_f32 v[234:235], v[188:189], s[30:31], v[98:99] op_sel_hi:[1,1,0]
	v_exp_f32_e32 v222, v222
	v_exp_f32_e32 v223, v223
	v_exp_f32_e32 v224, v224
	v_exp_f32_e32 v225, v225
	v_exp_f32_e32 v226, v226
	v_exp_f32_e32 v227, v227
	v_exp_f32_e32 v228, v228
	v_exp_f32_e32 v229, v229
	v_exp_f32_e32 v230, v230
	v_exp_f32_e32 v231, v231
	v_exp_f32_e32 v232, v232
	v_exp_f32_e32 v233, v233
	v_exp_f32_e32 v234, v234
	v_exp_f32_e32 v235, v235
	s_waitcnt vmcnt(16)
	v_mfma_f32_16x16x32_fp8_fp8 v[192:195], v[6:7], v[64:65], v[34:37]
	v_mfma_f32_16x16x32_fp8_fp8 v[196:199], v[8:9], v[64:65], v[22:25]
	s_waitcnt vmcnt(15)
	v_mfma_f32_16x16x32_fp8_fp8 v[200:203], v[2:3], v[64:65], v[38:41]
	v_mfma_f32_16x16x32_fp8_fp8 v[204:207], v[4:5], v[64:65], v[42:45]
	v_pk_add_f32 v[86:87], v[222:223], v[224:225]
	v_pk_add_f32 v[88:89], v[226:227], v[228:229]
	v_pk_add_f32 v[90:91], v[230:231], v[232:233]
	v_pk_mul_f32 v[92:93], v[222:223], v[176:177]
	v_pk_mul_f32 v[94:95], v[224:225], v[178:179]
	v_pk_add_f32 v[86:87], v[86:87], v[234:235]
	v_pk_add_f32 v[88:89], v[88:89], v[90:91]
	v_pk_fma_f32 v[92:93], v[226:227], v[180:181], v[92:93]
	v_pk_fma_f32 v[94:95], v[228:229], v[182:183], v[94:95]
	v_pk_add_f32 v[86:87], v[86:87], v[88:89]
	v_pk_fma_f32 v[92:93], v[230:231], v[184:185], v[92:93]
	v_pk_fma_f32 v[94:95], v[232:233], v[186:187], v[94:95]
	v_add_f32_e32 v86, v86, v87
	v_pk_fma_f32 v[92:93], v[234:235], v[188:189], v[92:93]
	v_rcp_f32_e32 v87, v86
	v_pk_add_f32 v[92:93], v[92:93], v[94:95]
	v_mul_f32_e32 v87, v55, v87
	v_add_f32_e32 v92, v92, v93
	v_mul_f32_e32 v108, v86, v87
	v_mul_f32_e32 v92, v92, v87
	v_mul_f32_e32 v101, 0x43800000, v87
	v_mul_f32_e32 v105, 0x3d800000, v92
	v_max3_f32 v86, v192, v193, v194
	v_max3_f32 v87, v195, v196, v197
	v_max3_f32 v88, v198, v199, v200
	v_max3_f32 v89, v201, v202, v203
	v_max3_f32 v86, v86, v204, v205
	v_max3_f32 v87, v87, v88, v89
	v_max_f32_e32 v96, v86, v87
	v_mul_f32_e32 v98, 0xbdb8aa3b, v96
	v_pk_fma_f32 v[236:237], v[192:193], s[30:31], v[98:99] op_sel_hi:[1,1,0]
	v_pk_fma_f32 v[238:239], v[194:195], s[30:31], v[98:99] op_sel_hi:[1,1,0]
	v_pk_fma_f32 v[240:241], v[196:197], s[30:31], v[98:99] op_sel_hi:[1,1,0]
	v_pk_fma_f32 v[242:243], v[198:199], s[30:31], v[98:99] op_sel_hi:[1,1,0]
	v_pk_fma_f32 v[244:245], v[200:201], s[30:31], v[98:99] op_sel_hi:[1,1,0]
	v_pk_fma_f32 v[246:247], v[202:203], s[30:31], v[98:99] op_sel_hi:[1,1,0]
	v_pk_fma_f32 v[248:249], v[204:205], s[30:31], v[98:99] op_sel_hi:[1,1,0]
	v_exp_f32_e32 v236, v236
	v_exp_f32_e32 v237, v237
	v_exp_f32_e32 v238, v238
	v_exp_f32_e32 v239, v239
	v_exp_f32_e32 v240, v240
	v_exp_f32_e32 v241, v241
	v_exp_f32_e32 v242, v242
	v_exp_f32_e32 v243, v243
	v_exp_f32_e32 v244, v244
	v_exp_f32_e32 v245, v245
	v_exp_f32_e32 v246, v246
	v_exp_f32_e32 v247, v247
	v_exp_f32_e32 v248, v248
	v_exp_f32_e32 v249, v249
	v_pk_add_f32 v[86:87], v[236:237], v[238:239]
	v_pk_add_f32 v[88:89], v[240:241], v[242:243]
	v_pk_add_f32 v[90:91], v[244:245], v[246:247]
	v_pk_mul_f32 v[92:93], v[236:237], v[192:193]
	v_pk_mul_f32 v[94:95], v[238:239], v[194:195]
	v_pk_add_f32 v[86:87], v[86:87], v[248:249]
	v_pk_add_f32 v[88:89], v[88:89], v[90:91]
	v_pk_fma_f32 v[92:93], v[240:241], v[196:197], v[92:93]
	v_pk_fma_f32 v[94:95], v[242:243], v[198:199], v[94:95]
	v_pk_add_f32 v[86:87], v[86:87], v[88:89]
	v_pk_fma_f32 v[92:93], v[244:245], v[200:201], v[92:93]
	v_pk_fma_f32 v[94:95], v[246:247], v[202:203], v[94:95]
	v_add_f32_e32 v86, v86, v87
	v_pk_fma_f32 v[92:93], v[248:249], v[204:205], v[92:93]
	v_rcp_f32_e32 v87, v86
	v_pk_add_f32 v[92:93], v[92:93], v[94:95]
	v_mul_f32_e32 v87, v55, v87
	v_add_f32_e32 v92, v92, v93
	v_mul_f32_e32 v109, v86, v87
	v_mul_f32_e32 v92, v92, v87
	v_mul_f32_e32 v102, 0x43800000, v87
	v_mul_f32_e32 v106, 0x3d800000, v92
	v_max3_f32 v122, v103, v105, v106
	v_cmp_gt_u32_e64 s[6:7], 16, v104
	v_mov_b32_e32 v123, v122
	s_nop 1
	v_permlane16_swap_b32_e32 v122, v123
	v_max_f32_e32 v122, v122, v123
	v_mov_b32_e32 v123, v122
	s_nop 1
	v_permlane32_swap_b32_e32 v122, v123
	v_max_f32_e32 v36, v122, v123
	v_mul_f32_e32 v123, 0x3fb8aa3b, v36
	v_fma_f32 v111, v103, v121, -v123
	v_exp_f32_e32 v111, v111
	s_nop 0
	v_mul_f32_e32 v112, v111, v100
	v_mul_f32_e32 v110, v111, v107
	v_mov_b32_e32 v114, v111
	v_pk_mul_f32 v[208:209], v[208:209], v[112:113] op_sel_hi:[1,0]
	v_pk_mul_f32 v[210:211], v[210:211], v[112:113] op_sel_hi:[1,0]
	v_pk_mul_f32 v[212:213], v[212:213], v[112:113] op_sel_hi:[1,0]
	v_pk_mul_f32 v[214:215], v[214:215], v[112:113] op_sel_hi:[1,0]
	v_pk_mul_f32 v[216:217], v[216:217], v[112:113] op_sel_hi:[1,0]
	v_pk_mul_f32 v[218:219], v[218:219], v[112:113] op_sel_hi:[1,0]
	v_pk_mul_f32 v[220:221], v[220:221], v[112:113] op_sel_hi:[1,0]
	s_waitcnt vmcnt(13)
	v_mov_b32_e32 v115, v110
	v_fma_mix_f32 v116, v110, v70, 0 op_sel_hi:[0,1,0]
	v_fma_mix_f32 v117, v110, v70, 0 op_sel:[0,1,0] op_sel_hi:[0,1,0]
	v_fma_mix_f32 v118, v110, v71, 0 op_sel_hi:[0,1,0]
	v_cvt_pk_fp8_f32 v72, v208, v209
	v_cvt_pk_fp8_f32 v73, v212, v213
	v_cvt_pk_fp8_f32 v74, v216, v217
	v_cvt_pk_fp8_f32 v75, v220, v221
	v_cvt_pk_fp8_f32 v72, v210, v211 op_sel:[0,0,1]
	v_cvt_pk_fp8_f32 v73, v214, v215 op_sel:[0,0,1]
	v_cvt_pk_fp8_f32 v74, v218, v219 op_sel:[0,0,1]
	s_nop 1
	v_mfma_f32_16x16x32_fp8_fp8 v[152:155], v[72:73], v[30:31], 0
	v_mfma_f32_16x16x32_fp8_fp8 v[152:155], v[74:75], v[32:33], v[152:155]
	v_fma_f32 v111, v105, v121, -v123
	v_exp_f32_e32 v111, v111
	s_nop 0
	v_mul_f32_e32 v112, v111, v101
	v_mul_f32_e32 v110, v111, v108
	v_add_f32_e32 v114, v114, v111
	v_pk_mul_f32 v[222:223], v[222:223], v[112:113] op_sel_hi:[1,0]
	v_pk_mul_f32 v[224:225], v[224:225], v[112:113] op_sel_hi:[1,0]
	v_pk_mul_f32 v[226:227], v[226:227], v[112:113] op_sel_hi:[1,0]
	v_pk_mul_f32 v[228:229], v[228:229], v[112:113] op_sel_hi:[1,0]
	v_pk_mul_f32 v[230:231], v[230:231], v[112:113] op_sel_hi:[1,0]
	v_pk_mul_f32 v[232:233], v[232:233], v[112:113] op_sel_hi:[1,0]
	v_pk_mul_f32 v[234:235], v[234:235], v[112:113] op_sel_hi:[1,0]
	s_waitcnt vmcnt(11)
	v_add_f32_e32 v115, v115, v110
	v_fma_mix_f32 v116, v110, v66, v116 op_sel_hi:[0,1,0]
	v_fma_mix_f32 v117, v110, v66, v117 op_sel:[0,1,0] op_sel_hi:[0,1,0]
	v_fma_mix_f32 v118, v110, v67, v118 op_sel_hi:[0,1,0]
	v_cvt_pk_fp8_f32 v76, v222, v223
	v_cvt_pk_fp8_f32 v77, v226, v227
	v_cvt_pk_fp8_f32 v78, v230, v231
	v_cvt_pk_fp8_f32 v79, v234, v235
	v_cvt_pk_fp8_f32 v76, v224, v225 op_sel:[0,0,1]
	v_cvt_pk_fp8_f32 v77, v228, v229 op_sel:[0,0,1]
	v_cvt_pk_fp8_f32 v78, v232, v233 op_sel:[0,0,1]
	s_nop 1
	v_mfma_f32_16x16x32_fp8_fp8 v[152:155], v[76:77], v[26:27], v[152:155]
	v_mfma_f32_16x16x32_fp8_fp8 v[152:155], v[78:79], v[28:29], v[152:155]
	v_fma_f32 v111, v106, v121, -v123
	v_exp_f32_e32 v111, v111
	s_nop 0
	v_mul_f32_e32 v112, v111, v102
	v_mul_f32_e32 v110, v111, v109
	v_add_f32_e32 v114, v114, v111
	v_pk_mul_f32 v[236:237], v[236:237], v[112:113] op_sel_hi:[1,0]
	v_pk_mul_f32 v[238:239], v[238:239], v[112:113] op_sel_hi:[1,0]
	v_pk_mul_f32 v[240:241], v[240:241], v[112:113] op_sel_hi:[1,0]
	v_pk_mul_f32 v[242:243], v[242:243], v[112:113] op_sel_hi:[1,0]
	v_pk_mul_f32 v[244:245], v[244:245], v[112:113] op_sel_hi:[1,0]
	v_pk_mul_f32 v[246:247], v[246:247], v[112:113] op_sel_hi:[1,0]
	v_pk_mul_f32 v[248:249], v[248:249], v[112:113] op_sel_hi:[1,0]
	s_waitcnt vmcnt(9)
	v_add_f32_e32 v115, v115, v110
	v_fma_mix_f32 v116, v110, v68, v116 op_sel_hi:[0,1,0]
	v_fma_mix_f32 v117, v110, v68, v117 op_sel:[0,1,0] op_sel_hi:[0,1,0]
	v_fma_mix_f32 v118, v110, v69, v118 op_sel_hi:[0,1,0]
	v_cvt_pk_fp8_f32 v80, v236, v237
	v_cvt_pk_fp8_f32 v81, v240, v241
	v_cvt_pk_fp8_f32 v82, v244, v245
	v_cvt_pk_fp8_f32 v83, v248, v249
	v_cvt_pk_fp8_f32 v80, v238, v239 op_sel:[0,0,1]
	v_cvt_pk_fp8_f32 v81, v242, v243 op_sel:[0,0,1]
	v_cvt_pk_fp8_f32 v82, v246, v247 op_sel:[0,0,1]
	s_nop 1
	v_mfma_f32_16x16x32_fp8_fp8 v[152:155], v[80:81], v[18:19], v[152:155]
	v_mfma_f32_16x16x32_fp8_fp8 v[152:155], v[82:83], v[20:21], v[152:155]
	v_mov_b32_e32 v86, v114
	v_mov_b32_e32 v87, v115
	v_mov_b32_e32 v88, v116
	v_mov_b32_e32 v89, v117
	v_mov_b32_e32 v90, v118
	v_permlane16_swap_b32_e32 v114, v86
	v_permlane16_swap_b32_e32 v115, v87
	v_permlane16_swap_b32_e32 v116, v88
	v_permlane16_swap_b32_e32 v117, v89
	v_permlane16_swap_b32_e32 v118, v90
	v_add_f32_e32 v114, v114, v86
	v_add_f32_e32 v115, v115, v87
	v_add_f32_e32 v116, v116, v88
	v_add_f32_e32 v117, v117, v89
	v_add_f32_e32 v118, v118, v90
	v_mov_b32_e32 v86, v114
	v_mov_b32_e32 v87, v115
	v_mov_b32_e32 v88, v116
	v_mov_b32_e32 v89, v117
	v_mov_b32_e32 v90, v118
	v_permlane32_swap_b32_e32 v114, v86
	v_permlane32_swap_b32_e32 v115, v87
	v_permlane32_swap_b32_e32 v116, v88
	v_permlane32_swap_b32_e32 v117, v89
	v_permlane32_swap_b32_e32 v118, v90
	v_add_f32_e32 v37, v114, v86
	v_add_f32_e32 v20, v115, v87
	v_add_f32_e32 v18, v116, v88
	v_add_f32_e32 v19, v117, v89
	v_add_f32_e32 v21, v118, v90
	ds_write2_b32 v156, v152, v153 offset0:0 offset1:20
	ds_write2_b32 v156, v154, v155 offset0:40 offset1:60
	s_branch .LBB1_30
.LBB1_16:
	s_mov_b32 exec_lo, 0x1ff01ff
	s_mov_b32 exec_hi, 0x1ff01ff
	global_load_dword v120, v144, s[10:11]
	s_mov_b32 exec_lo, 0xe000e00
	s_mov_b32 exec_hi, 0xe000e00
	global_load_dword v120, v145, s[12:13]
	s_mov_b32 exec_lo, 0x70007000
	s_mov_b32 exec_hi, 0x70007000
	global_load_dword v120, v146, s[14:15]
	s_mov_b64 exec, -1
	global_load_dwordx4 v[124:127], v147, s[22:23]
	global_load_dwordx4 v[128:131], v148, s[22:23]
	s_mov_b32 exec_hi, 0
	global_load_dwordx4 v[132:135], v149, s[16:17]
	s_mov_b32 exec_hi, -1
	s_mov_b32 exec_lo, 0
	global_load_dwordx4 v[132:135], v149, s[18:19] offset:-512
	s_mov_b32 exec_lo, -1
	global_load_dwordx4 v[136:139], v150, s[8:9]
	global_load_dwordx4 v[140:143], v150, s[8:9] offset:256
	v_mov_b32_e32 v21, 0
	ds_write2_b32 v156, v21, v21 offset1:20
	ds_write2_b32 v156, v21, v21 offset0:40 offset1:60
	v_cmp_gt_u32_e64 s[6:7], 16, v104
	v_mov_b32_e32 v37, 1.0
	v_mov_b32_e32 v20, 0
	v_mov_b32_e32 v19, 0
	v_mov_b32_e32 v18, 0
	v_mov_b32_e32 v36, 0
